# static s_setprio 1 for waves 4-7 in the diff-attention loop + SSD load hoists
# baseline (speedup 1.0000x reference)
.LBB0_564:
	s_xor_b64 s[12:13], s[14:15], -1
	s_and_b64 s[14:15], s[14:15], exec
	s_cselect_b32 s39, s31, s34
	s_mul_i32 s14, s39, 0x1a00
	v_mov_b32_e32 v128, v231
	s_add_u32 s16, s6, s14
	s_addc_u32 s17, s7, 0
	v_readfirstlane_b32 s18, v128
	v_lshlrev_b32_e32 v0, 3, v128
	s_ashr_i32 s14, s18, 6
	v_and_b32_e32 v129, 0x78, v0
	v_bfe_u32 v130, v128, 4, 2
	s_lshl_b32 s38, s14, 5
	v_lshlrev_b32_e32 v208, 1, v129
	v_or_b32_e32 v2, 4, v130
	v_or_b32_e32 v8, 8, v130
	v_or_b32_e32 v10, 12, v130
	v_lshl_add_u64 v[28:29], s[16:17], 0, v[208:209]
	v_or_b32_e32 v32, s38, v130
	v_or_b32_e32 v33, s38, v2
	v_or_b32_e32 v34, s38, v8
	v_or_b32_e32 v35, s38, v10
	v_mad_i64_i32 v[0:1], s[16:17], v32, s62, v[28:29]
	v_mad_i64_i32 v[4:5], s[16:17], v33, s62, v[28:29]
	v_mad_i64_i32 v[8:9], s[16:17], v34, s62, v[28:29]
	v_mad_i64_i32 v[12:13], s[16:17], v35, s62, v[28:29]
	global_load_dwordx4 v[0:3], v[0:1], off
	s_nop 0
	global_load_dwordx4 v[4:7], v[4:5], off
	s_nop 0
	global_load_dwordx4 v[8:11], v[8:9], off
	s_nop 0
	global_load_dwordx4 v[12:15], v[12:13], off
	v_or_b32_e32 v36, 16, v32
	v_mad_i64_i32 v[16:17], s[16:17], v36, s62, v[28:29]
	global_load_dwordx4 v[16:19], v[16:17], off
	v_or_b32_e32 v20, 20, v130
	v_or_b32_e32 v37, s38, v20
	v_mad_i64_i32 v[20:21], s[16:17], v37, s62, v[28:29]
	global_load_dwordx4 v[20:23], v[20:21], off
	v_or_b32_e32 v24, 24, v130
	v_or_b32_e32 v38, s38, v24
	v_mad_i64_i32 v[24:25], s[16:17], v38, s62, v[28:29]
	v_or_b32_e32 v30, 28, v130
	global_load_dwordx4 v[24:27], v[24:25], off
	v_or_b32_e32 v39, s38, v30
	v_mad_i64_i32 v[28:29], s[16:17], v39, s62, v[28:29]
	global_load_dwordx4 v[28:31], v[28:29], off
	v_xor_b32_e32 v40, v130, v128
	v_bitop3_b32 v41, v130, v128, 4 bitop3:0x36
	v_bitop3_b32 v42, v130, v128, 8 bitop3:0x36
	v_bitop3_b32 v43, v130, v128, 12 bitop3:0x36
	v_lshlrev_b32_e32 v40, 4, v40
	v_lshlrev_b32_e32 v41, 4, v41
	v_lshlrev_b32_e32 v42, 4, v42
	v_lshlrev_b32_e32 v43, 4, v43
	v_and_b32_e32 v40, 0xf0, v40
	v_lshlrev_b32_e32 v32, 8, v32
	v_and_b32_e32 v41, 0xf0, v41
	v_and_b32_e32 v42, 0xf0, v42
	v_and_b32_e32 v43, 0xf0, v43
	v_lshlrev_b32_e32 v33, 8, v33
	v_lshlrev_b32_e32 v34, 8, v34
	v_lshlrev_b32_e32 v35, 8, v35
	v_add3_u32 v32, s65, v32, v40
	s_and_b32 s16, s18, 0x3fffffc0
	v_add3_u32 v33, s65, v33, v41
	v_add3_u32 v34, s65, v34, v42
	v_add3_u32 v35, s65, v35, v43
	v_lshlrev_b32_e32 v36, 8, v36
	s_lshl_b32 s16, s16, 2
	s_add_i32 s40, s16, 0
	s_lshl_b32 s16, s14, 3
	v_bitop3_b32 v56, s16, v128, v130 bitop3:0x36
	v_or_b32_e32 v55, s16, v130
	v_lshlrev_b32_e32 v56, 3, v56
	v_mul_lo_u32 v57, v55, s96
	v_and_b32_e32 v133, 0x78, v56
	v_bitop3_b32 v55, v55, v128, 4 bitop3:0x36
	v_lshlrev_b32_e32 v132, 5, v130
	v_or_b32_e32 v56, v133, v57
	v_lshlrev_b32_e32 v55, 3, v55
	v_lshlrev_b32_e32 v208, 1, v56
	v_bitop3_b32 v56, v57, v132, v129 bitop3:0xf6
	v_add_u32_e32 v57, 0x3400, v57
	s_waitcnt vmcnt(7)
	ds_write_b128 v32, v[0:3]
	s_waitcnt vmcnt(6)
	ds_write_b128 v33, v[4:7]
	s_waitcnt vmcnt(5)
	ds_write_b128 v34, v[8:11]
	s_waitcnt vmcnt(4)
	ds_write_b128 v35, v[12:15]
	v_bitop3_b32 v1, v130, v128, 20 bitop3:0x36
	v_add3_u32 v0, s65, v36, v40
	v_lshlrev_b32_e32 v1, 4, v1
	s_waitcnt vmcnt(3)
	ds_write_b128 v0, v[16:19]
	v_lshlrev_b32_e32 v0, 8, v37
	v_and_b32_e32 v1, 0xf0, v1
	v_add3_u32 v0, s65, v0, v1
	v_bitop3_b32 v1, v130, v128, 24 bitop3:0x36
	v_lshlrev_b32_e32 v1, 4, v1
	s_waitcnt vmcnt(2)
	ds_write_b128 v0, v[20:23]
	v_lshlrev_b32_e32 v0, 8, v38
	v_and_b32_e32 v1, 0xf0, v1
	v_add3_u32 v0, s65, v0, v1
	v_bitop3_b32 v1, v130, v128, 28 bitop3:0x36
	v_lshlrev_b32_e32 v1, 4, v1
	v_and_b32_e32 v134, 0x78, v55
	s_waitcnt vmcnt(1)
	ds_write_b128 v0, v[24:27]
	v_lshlrev_b32_e32 v0, 8, v39
	v_and_b32_e32 v1, 0xf0, v1
	v_or_b32_e32 v55, v134, v57
	s_lshl_b32 s16, s14, 11
	v_add3_u32 v0, s65, v0, v1
	v_lshlrev_b32_e32 v56, 1, v56
	v_lshlrev_b32_e32 v58, 1, v55
	v_bitop3_b32 v55, v57, v132, v129 bitop3:0xf6
	v_lshl_add_u64 v[62:63], s[6:7], 0, v[208:209]
	s_add_i32 s44, s16, 0
	v_mov_b32_e32 v57, v209
	s_waitcnt vmcnt(0)
	ds_write_b128 v0, v[28:31]
	v_mov_b32_e32 v64, v209
	v_mov_b32_e32 v32, v209
	v_mov_b32_e32 v16, v209
	v_mov_b32_e32 v0, v209
	v_mov_b32_e32 v112, v209
	v_mov_b32_e32 v96, v209
	v_mov_b32_e32 v80, v209
	v_mov_b32_e32 v48, v209
	v_lshl_add_u64 v[62:63], v[62:63], 0, s[86:87]
	s_mov_b32 m0, s44
	v_lshl_add_u64 v[56:57], s[6:7], 0, v[56:57]
	global_load_lds_dwordx4 v[62:63], off
	v_lshl_add_u64 v[56:57], v[56:57], 0, s[88:89]
	s_add_i32 m0, s44, 0x8000
	v_mov_b32_e32 v59, v209
	global_load_lds_dwordx4 v[56:57], off
	v_lshl_add_u64 v[56:57], s[6:7], 0, v[58:59]
	v_lshlrev_b32_e32 v60, 1, v55
	v_lshl_add_u64 v[56:57], v[56:57], 0, s[86:87]
	s_add_i32 m0, s44, 0x400
	v_mov_b32_e32 v61, v209
	global_load_lds_dwordx4 v[56:57], off
	v_lshl_add_u64 v[56:57], s[6:7], 0, v[60:61]
	v_lshl_add_u64 v[56:57], v[56:57], 0, s[88:89]
	s_add_i32 m0, s44, 0x8400
	v_bfe_u32 v135, v128, 5, 1
	global_load_lds_dwordx4 v[56:57], off
	v_and_b32_e32 v235, 63, v128
	v_and_b32_e32 v131, 31, v128
	v_and_b32_e32 v136, 15, v128
	v_bfe_u32 v137, v128, 2, 2
	v_and_b32_e32 v139, 16, v128
	v_lshlrev_b32_e32 v140, 2, v128
	v_bitop3_b32 v128, v135, v128, 15 bitop3:0x78
	v_lshlrev_b32_e32 v240, 4, v128
	v_bitop3_b32 v128, v135, v136, 2 bitop3:0x36
	v_lshlrev_b32_e32 v241, 4, v128
	v_bitop3_b32 v128, v135, v136, 4 bitop3:0x36
	v_lshlrev_b32_e32 v242, 4, v128
	v_bitop3_b32 v128, v135, v136, 6 bitop3:0x36
	v_lshlrev_b32_e32 v243, 4, v128
	v_bitop3_b32 v128, v135, v136, 8 bitop3:0x36
	v_lshlrev_b32_e32 v244, 4, v128
	v_bitop3_b32 v128, v135, v136, 10 bitop3:0x36
	v_lshlrev_b32_e32 v245, 4, v128
	v_bitop3_b32 v128, v135, v136, 12 bitop3:0x36
	s_add_i32 s16, s38, s39
	v_lshlrev_b32_e32 v246, 4, v128
	v_bitop3_b32 v128, v135, v136, 14 bitop3:0x36
	v_or_b32_e32 v44, s38, v131
	s_add_i32 s40, s40, 0x10000
	v_lshl_add_u32 v237, v131, 8, 0
	v_lshlrev_b32_e32 v247, 4, v128
	v_lshlrev_b32_e32 v128, 4, v135
	v_add_lshl_u32 v131, s16, v131, 2
	v_add_u32_e32 v249, s40, v128
	v_sub_u32_e32 v128, v128, v131
	s_mulk_i32 s14, 0x6800
	v_add_u32_e32 v250, s97, v128
	v_mov_b32_e32 v128, s14
	v_mad_u32_u24 v128, v130, s96, v128
	v_or_b32_e32 v131, v128, v133
	s_addk_i32 s14, 0x3400
	v_lshlrev_b32_e32 v208, 1, v131
	v_mov_b32_e32 v131, s14
	v_mad_u32_u24 v130, v130, s96, v131
	v_or_b32_e32 v130, v130, v134
	s_ashr_i32 s17, s16, 31
	v_lshl_add_u64 v[210:211], s[8:9], 0, v[208:209]
	v_lshlrev_b32_e32 v208, 1, v130
	v_bitop3_b32 v128, v132, v128, v129 bitop3:0xde
	s_lshr_b32 s15, s39, 6
	s_lshr_b32 s17, s17, 26
	v_lshlrev_b32_e32 v138, 8, v137
	v_and_or_b32 v139, v140, 12, v139
	v_lshl_add_u64 v[216:217], s[8:9], 0, v[208:209]
	v_lshlrev_b32_e32 v208, 1, v128
	s_add_i32 s42, s15, 4
	s_add_i32 s17, s16, s17
	v_lshl_or_b32 v138, v135, 10, v138
	v_lshlrev_b32_e32 v139, 1, v139
	s_mul_i32 s15, s15, 0x68000
	v_lshl_add_u64 v[218:219], s[10:11], 0, v[208:209]
	v_add_u32_e32 v208, 0x6800, v208
	s_mov_b32 s41, 1
	v_lshl_add_u32 v236, v44, 8, s65
	s_mov_b32 s43, 0
	v_mov_b32_e32 v65, v64
	v_mov_b32_e32 v66, v64
	v_mov_b32_e32 v67, v64
	v_mov_b32_e32 v68, v64
	v_mov_b32_e32 v69, v64
	v_mov_b32_e32 v70, v64
	v_mov_b32_e32 v71, v64
	v_mov_b32_e32 v72, v64
	v_mov_b32_e32 v73, v64
	v_mov_b32_e32 v74, v64
	v_mov_b32_e32 v75, v64
	v_mov_b32_e32 v76, v64
	v_mov_b32_e32 v77, v64
	v_mov_b32_e32 v78, v64
	v_mov_b32_e32 v79, v64
	v_mov_b32_e32 v33, v32
	v_mov_b32_e32 v34, v32
	v_mov_b32_e32 v35, v32
	v_mov_b32_e32 v36, v32
	v_mov_b32_e32 v37, v32
	v_mov_b32_e32 v38, v32
	v_mov_b32_e32 v39, v32
	v_mov_b32_e32 v40, v32
	v_mov_b32_e32 v41, v32
	v_mov_b32_e32 v42, v32
	v_mov_b32_e32 v43, v32
	v_mov_b32_e32 v44, v32
	v_mov_b32_e32 v45, v32
	v_mov_b32_e32 v46, v32
	v_mov_b32_e32 v47, v32
	v_mov_b32_e32 v17, v16
	v_mov_b32_e32 v18, v16
	v_mov_b32_e32 v19, v16
	v_mov_b32_e32 v20, v16
	v_mov_b32_e32 v21, v16
	v_mov_b32_e32 v22, v16
	v_mov_b32_e32 v23, v16
	v_mov_b32_e32 v24, v16
	v_mov_b32_e32 v25, v16
	v_mov_b32_e32 v26, v16
	v_mov_b32_e32 v27, v16
	v_mov_b32_e32 v28, v16
	v_mov_b32_e32 v29, v16
	v_mov_b32_e32 v30, v16
	v_mov_b32_e32 v31, v16
	v_mov_b32_e32 v1, v0
	v_mov_b32_e32 v2, v0
	v_mov_b32_e32 v3, v0
	v_mov_b32_e32 v4, v0
	v_mov_b32_e32 v5, v0
	v_mov_b32_e32 v6, v0
	v_mov_b32_e32 v7, v0
	v_mov_b32_e32 v8, v0
	v_mov_b32_e32 v9, v0
	v_mov_b32_e32 v10, v0
	v_mov_b32_e32 v11, v0
	v_mov_b32_e32 v12, v0
	v_mov_b32_e32 v13, v0
	v_mov_b32_e32 v14, v0
	v_mov_b32_e32 v15, v0
	v_mov_b32_e32 v113, v112
	v_mov_b32_e32 v114, v112
	v_mov_b32_e32 v115, v112
	v_mov_b32_e32 v116, v112
	v_mov_b32_e32 v117, v112
	v_mov_b32_e32 v118, v112
	v_mov_b32_e32 v119, v112
	v_mov_b32_e32 v120, v112
	v_mov_b32_e32 v121, v112
	v_mov_b32_e32 v122, v112
	v_mov_b32_e32 v123, v112
	v_mov_b32_e32 v124, v112
	v_mov_b32_e32 v125, v112
	v_mov_b32_e32 v126, v112
	v_mov_b32_e32 v127, v112
	v_mov_b32_e32 v97, v96
	v_mov_b32_e32 v98, v96
	v_mov_b32_e32 v99, v96
	v_mov_b32_e32 v100, v96
	v_mov_b32_e32 v101, v96
	v_mov_b32_e32 v102, v96
	v_mov_b32_e32 v103, v96
	v_mov_b32_e32 v104, v96
	v_mov_b32_e32 v105, v96
	v_mov_b32_e32 v106, v96
	v_mov_b32_e32 v107, v96
	v_mov_b32_e32 v108, v96
	v_mov_b32_e32 v109, v96
	v_mov_b32_e32 v110, v96
	v_mov_b32_e32 v111, v96
	v_mov_b32_e32 v81, v80
	v_mov_b32_e32 v82, v80
	v_mov_b32_e32 v83, v80
	v_mov_b32_e32 v84, v80
	v_mov_b32_e32 v85, v80
	v_mov_b32_e32 v86, v80
	v_mov_b32_e32 v87, v80
	v_mov_b32_e32 v88, v80
	v_mov_b32_e32 v89, v80
	v_mov_b32_e32 v90, v80
	v_mov_b32_e32 v91, v80
	v_mov_b32_e32 v92, v80
	v_mov_b32_e32 v93, v80
	v_mov_b32_e32 v94, v80
	v_mov_b32_e32 v95, v80
	v_mov_b32_e32 v49, v48
	v_mov_b32_e32 v50, v48
	v_mov_b32_e32 v51, v48
	v_mov_b32_e32 v52, v48
	v_mov_b32_e32 v53, v48
	v_mov_b32_e32 v54, v48
	v_mov_b32_e32 v55, v48
	v_mov_b32_e32 v56, v48
	v_mov_b32_e32 v57, v48
	v_mov_b32_e32 v58, v48
	v_mov_b32_e32 v59, v48
	v_mov_b32_e32 v60, v48
	v_mov_b32_e32 v61, v48
	v_mov_b32_e32 v62, v48
	v_mov_b32_e32 v63, v48
	s_ashr_i32 s45, s17, 6
	v_add3_u32 v238, 0, v138, v139
	v_lshl_add_u32 v239, v235, 2, s40
	v_lshlrev_b32_e32 v248, 6, v137
	s_add_u32 s46, s15, 0x1a0000
	v_lshl_add_u64 v[220:221], s[10:11], 0, v[208:209]
	s_sub_i32 s47, 0, s16
	v_mov_b32_e32 v226, 0xff800000
	v_mov_b32_e32 v251, 0
	s_mov_b64 s[14:15], 0
	v_mov_b32_e32 v208, 0
	v_mov_b32_e32 v227, 0xff800000
	s_add_i32 m0, s44, 0x4000
	s_nop 0
	global_load_lds_dwordx4 v[210:211], off
	s_add_i32 m0, s44, 0x4400
	s_nop 0
	global_load_lds_dwordx4 v[216:217], off
	s_waitcnt vmcnt(0) lgkmcnt(0)
	s_barrier
	s_cmp_ge_u32 s38, 0x80
	s_cbranch_scc0 .Lattn_noprio
	s_setprio 1
.Lattn_noprio:
	s_mov_b32 s48, 0
	v_mov_b32_e32 v228, s64
	ds_read_b32 v229, v228
	v_add3_u32 v254, v237, v240, s48
	ds_read_b128 v[128:131], v254
	ds_read_b128 v[132:135], v254 offset:8192
	v_add_u32_e32 v255, v236, v240
	ds_read_b128 v[136:139], v255
	v_add3_u32 v254, v237, v241, s48
	ds_read_b128 v[140:143], v254
	ds_read_b128 v[144:147], v254 offset:8192
	v_add_u32_e32 v255, v236, v241
	ds_read_b128 v[148:151], v255
	v_add3_u32 v254, v237, v242, s48
	ds_read_b128 v[152:155], v254
	ds_read_b128 v[156:159], v254 offset:8192
	v_add_u32_e32 v255, v236, v242
	ds_read_b128 v[192:195], v255
	v_add3_u32 v254, v237, v243, s48
	ds_read_b128 v[196:199], v254
	ds_read_b128 v[200:203], v254 offset:8192
	v_add_u32_e32 v255, v236, v243
	ds_read_b128 v[204:207], v255
	s_waitcnt lgkmcnt(9)
	v_mfma_f32_32x32x16_bf16 v[160:175], v[128:131], v[136:139], 0
	v_mfma_f32_32x32x16_bf16 v[176:191], v[132:135], v[136:139], 0
	s_waitcnt lgkmcnt(6)
	v_mfma_f32_32x32x16_bf16 v[160:175], v[140:143], v[148:151], v[160:175]
	v_mfma_f32_32x32x16_bf16 v[176:191], v[144:147], v[148:151], v[176:191]
	s_waitcnt lgkmcnt(3)
	v_mfma_f32_32x32x16_bf16 v[160:175], v[152:155], v[192:195], v[160:175]
	v_mfma_f32_32x32x16_bf16 v[176:191], v[156:159], v[192:195], v[176:191]
	s_waitcnt lgkmcnt(0)
	v_mfma_f32_32x32x16_bf16 v[160:175], v[196:199], v[204:207], v[160:175]
	v_mfma_f32_32x32x16_bf16 v[176:191], v[200:203], v[204:207], v[176:191]
	v_readfirstlane_b32 s50, v229

.Lattn_done:
	s_setprio 0
	s_branch .LBB0_563
